# mixer-phase work queue order: two conversion chunks per mixer unit while chunks last (conversions finish earlier, the tail is made of cheap mixer units)
# speedup vs baseline: 1.0093x; 1.0093x over previous
.LBB0_893:
	s_or_b64 exec, exec, s[36:37]
	v_readlane_b32 s2, v255, 15
	s_waitcnt lgkmcnt(0)
	s_barrier
	v_mov_b32_e32 v0, s2
	ds_read_b32 v0, v0
	s_and_b64 s[2:3], s[70:71], exec
	s_movk_i32 s2, 0x3a8
	s_cselect_b32 s27, s2, 0x270
	s_or_b32 s97, s27, 0x400
	s_waitcnt lgkmcnt(0)
	v_cmp_le_u32_e32 vcc, s97, v0
	v_readfirstlane_b32 s7, v0
	s_cbranch_vccnz .LBB0_1552
	s_add_u32 s72, s20, 0x40200000
	s_addc_u32 s73, s21, 0
	s_add_u32 s80, s20, 0x53800000
	v_writelane_b32 v255, s78, 40
	s_addc_u32 s81, s21, 0
	s_add_u32 s2, s20, 0x53600000
	v_writelane_b32 v255, s79, 41
	v_writelane_b32 v255, s2, 42
	s_addc_u32 s2, s21, 0
	v_writelane_b32 v255, s2, 43
	v_writelane_b32 v255, s70, 44
	s_and_b64 s[2:3], s[70:71], exec
	s_movk_i32 s2, 0x4e00
	v_writelane_b32 v255, s71, 45
	s_cselect_b32 s78, s2, 0x13800
	v_readlane_b32 s2, v255, 36
	v_readlane_b32 s3, v255, 37
	s_lshr_b32 s79, s27, 1
	s_add_i32 s79, s79, s27
	s_lshl_b32 s3, s2, 4
	s_lshl_b32 s2, s2, 3
	s_add_u32 s71, s20, 0x24200000
	v_writelane_b32 v255, s3, 46
	s_addc_u32 s23, s21, 0
	v_writelane_b32 v255, s2, 47
	s_add_u32 s2, s20, 0x90000
	v_writelane_b32 v255, s2, 48
	s_addc_u32 s2, s21, 0
	s_add_u32 s70, s20, 0x14200000
	v_writelane_b32 v255, s2, 49
	s_addc_u32 s2, s21, 0
	s_add_u32 s16, s20, 0x10200000
	s_addc_u32 s3, s21, 0
	s_add_u32 s74, s20, 0xd200000
	s_addc_u32 s75, s21, 0
	s_add_u32 s30, s20, 0x110000
	s_addc_u32 s31, s21, 0
	s_add_u32 s17, s20, 0x200000
	s_addc_u32 s12, s21, 0
	s_add_u32 s13, s20, 0x137000
	s_addc_u32 s5, s21, 0
	s_add_u32 s34, s20, 0x2a00000
	v_readlane_b32 s8, v255, 11
	s_addc_u32 s35, s21, 0
	s_add_i32 s8, s78, s8
	v_writelane_b32 v255, s8, 50
	s_add_i32 s83, s78, 0xffffb200
	v_readlane_b32 s8, v255, 9
	s_add_i32 s8, s8, s78
	v_mov_b32_e32 v213, 0
	v_writelane_b32 v255, s8, 51
	s_nop 0
	v_readlane_b32 s8, v255, 10
	s_add_i32 s8, s8, s78
	s_nop 0
	v_writelane_b32 v255, s8, 52
	s_nop 0
	v_readlane_b32 s8, v255, 12
	s_add_i32 s8, s8, s78
	s_nop 0
	v_writelane_b32 v255, s8, 53
	s_branch .LBB0_896

.LBB0_917:
	s_mul_hi_u32 s8, s7, 0xaaaaaaab
	s_lshr_b32 s8, s8, 1
	s_mul_i32 s10, s8, 3
	s_sub_i32 s10, s7, s10
	s_lshl_b32 s7, s8, 1
	s_add_i32 s7, s7, s10
	s_add_i32 s7, s7, -1
	s_cmp_eq_u32 s10, 0
	s_cselect_b32 s26, -1, s7
	s_cselect_b32 s28, s8, -1
	s_cmp_lt_i32 s26, 0
	s_mov_b64 s[38:39], -1
	s_cbranch_scc1 .LBB0_903
